# speedup vs baseline: 1.0129x; 1.0129x over previous
.LBB2_21:
	v_cvt_pk_f16_f32 v13, v13, v13
	v_cvt_pk_f16_f32 v12, v12, v12
	v_cvt_pk_f16_f32 v11, v11, v11
	v_cvt_pk_f16_f32 v10, v10, v10
	ds_write_b128 v98, v[10:13]
	ds_write_b32 v98, v17 offset:16
	s_and_saveexec_b64 s[6:7], s[4:5]
	ds_write_b32 v99, v86 offset:16
	s_or_b64 exec, exec, s[6:7]
	s_sub_i32 s6, s23, s24
	s_cmp_lt_i32 s6, 1
	s_cbranch_scc1 .LBB2_26
	ds_read2_b32 v[10:11], v96 offset0:20 offset1:28
	ds_read2_b32 v[12:13], v96 offset0:4 offset1:12
	s_min_i32 s6, s6, 16
	s_mov_b32 s7, 0
	v_mov_b32_e32 v118, v96
	s_waitcnt lgkmcnt(1)
	v_lshl_or_b32 v58, v11, 8, v72
	s_waitcnt lgkmcnt(0)
	v_lshl_or_b32 v12, v12, 8, v72
	v_lshl_or_b32 v13, v13, 8, v72
	v_lshl_or_b32 v54, v10, 8, v72
	global_load_dwordx4 v[14:17], v12, s[16:17]
	s_nop 0
	global_load_dwordx4 v[10:13], v13, s[16:17]
	s_nop 0
	global_load_dwordx4 v[54:57], v54, s[16:17]
	s_nop 0
	global_load_dwordx4 v[58:61], v58, s[16:17]
.LBB2_25:
	ds_read_b128 v[120:123], v118
	ds_read_b128 v[124:127], v118 offset:32
	ds_read2_b32 v[6:7], v118 offset0:36 offset1:44
	s_add_i32 s7, s7, 4
	s_cmp_ge_i32 s7, s6
	s_waitcnt vmcnt(3) lgkmcnt(2)
	v_pk_fma_f16 v109, v14, v120, v109
	v_pk_fma_f16 v97, v14, v121, v97
	v_pk_fma_f16 v90, v14, v122, v90
	v_pk_fma_f16 v85, v14, v123, v85
	v_pk_fma_f16 v108, v15, v120, v108
	v_pk_fma_f16 v95, v15, v121, v95
	v_pk_fma_f16 v89, v15, v122, v89
	v_pk_fma_f16 v84, v15, v123, v84
	v_pk_fma_f16 v107, v16, v120, v107
	v_pk_fma_f16 v94, v16, v121, v94
	v_pk_fma_f16 v88, v16, v122, v88
	v_pk_fma_f16 v82, v16, v123, v82
	v_pk_fma_f16 v105, v17, v120, v105
	v_pk_fma_f16 v92, v17, v121, v92
	v_pk_fma_f16 v87, v17, v122, v87
	v_pk_fma_f16 v81, v17, v123, v81
	s_waitcnt lgkmcnt(0)
	v_lshl_or_b32 v14, v6, 8, v72
	global_load_dwordx4 v[14:17], v14, s[16:17]
	ds_read_b128 v[120:123], v118 offset:64
	s_waitcnt vmcnt(3)
	v_pk_fma_f16 v109, v10, v124, v109
	v_pk_fma_f16 v97, v10, v125, v97
	v_pk_fma_f16 v90, v10, v126, v90
	v_pk_fma_f16 v85, v10, v127, v85
	v_pk_fma_f16 v108, v11, v124, v108
	v_pk_fma_f16 v95, v11, v125, v95
	v_pk_fma_f16 v89, v11, v126, v89
	v_pk_fma_f16 v84, v11, v127, v84
	v_pk_fma_f16 v107, v12, v124, v107
	v_pk_fma_f16 v94, v12, v125, v94
	v_pk_fma_f16 v88, v12, v126, v88
	v_pk_fma_f16 v82, v12, v127, v82
	v_pk_fma_f16 v105, v13, v124, v105
	v_pk_fma_f16 v92, v13, v125, v92
	v_pk_fma_f16 v87, v13, v126, v87
	v_pk_fma_f16 v81, v13, v127, v81
	v_lshl_or_b32 v10, v7, 8, v72
	global_load_dwordx4 v[10:13], v10, s[16:17]
	ds_read2_b32 v[8:9], v118 offset0:52 offset1:60
	ds_read_b128 v[124:127], v118 offset:96
	s_waitcnt vmcnt(3) lgkmcnt(2)
	v_pk_fma_f16 v109, v54, v120, v109
	v_pk_fma_f16 v97, v54, v121, v97
	v_pk_fma_f16 v90, v54, v122, v90
	v_pk_fma_f16 v85, v54, v123, v85
	v_pk_fma_f16 v108, v55, v120, v108
	v_pk_fma_f16 v95, v55, v121, v95
	v_pk_fma_f16 v89, v55, v122, v89
	v_pk_fma_f16 v84, v55, v123, v84
	v_pk_fma_f16 v107, v56, v120, v107
	v_pk_fma_f16 v94, v56, v121, v94
	v_pk_fma_f16 v88, v56, v122, v88
	v_pk_fma_f16 v82, v56, v123, v82
	v_pk_fma_f16 v105, v57, v120, v105
	v_pk_fma_f16 v92, v57, v121, v92
	v_pk_fma_f16 v87, v57, v122, v87
	v_pk_fma_f16 v81, v57, v123, v81
	s_waitcnt lgkmcnt(1)
	v_lshl_or_b32 v54, v8, 8, v72
	global_load_dwordx4 v[54:57], v54, s[16:17]
	v_add_u32_e32 v118, 0x80, v118
	s_waitcnt vmcnt(3) lgkmcnt(0)
	v_pk_fma_f16 v109, v58, v124, v109
	v_pk_fma_f16 v97, v58, v125, v97
	v_pk_fma_f16 v90, v58, v126, v90
	v_pk_fma_f16 v85, v58, v127, v85
	v_pk_fma_f16 v108, v59, v124, v108
	v_pk_fma_f16 v95, v59, v125, v95
	v_pk_fma_f16 v89, v59, v126, v89
	v_pk_fma_f16 v84, v59, v127, v84
	v_pk_fma_f16 v107, v60, v124, v107
	v_pk_fma_f16 v94, v60, v125, v94
	v_pk_fma_f16 v88, v60, v126, v88
	v_pk_fma_f16 v82, v60, v127, v82
	v_pk_fma_f16 v105, v61, v124, v105
	v_pk_fma_f16 v92, v61, v125, v92
	v_pk_fma_f16 v87, v61, v126, v87
	v_pk_fma_f16 v81, v61, v127, v81
	v_lshl_or_b32 v58, v9, 8, v72
	global_load_dwordx4 v[58:61], v58, s[16:17]
	s_cbranch_scc0 .LBB2_25
